# baseline (speedup 1.0000x reference)
.LBB1_36:
	s_or_b64 exec, exec, s[2:3]
	s_waitcnt vmcnt(0)
	v_add_f32_e32 v103, 0, v103
	v_add_f32_e32 v103, v103, v104
	v_add_f32_e32 v103, v103, v105
	v_add_f32_e32 v103, v103, v106
	v_add_f32_e32 v103, v103, v107
	v_add_f32_e32 v103, v103, v108
	v_add_f32_e32 v103, v103, v109
	v_add_f32_e32 v103, v103, v110
	v_add_f32_e32 v103, v103, v111
	v_add_f32_e32 v103, v103, v112
	v_add_f32_e32 v103, v103, v113
	v_add_f32_e32 v103, v103, v114
	v_add_f32_e32 v103, v103, v115
	v_add_f32_e32 v103, v103, v116
	v_add_f32_e32 v103, v103, v117
	v_add_f32_e32 v103, v103, v118
	v_add_f32_e32 v103, v103, v119
	v_add_f32_e32 v103, v103, v120
	v_add_f32_e32 v103, v103, v121
	v_add_f32_e32 v103, v103, v122
	s_mov_b32 s14, 0xf800000
	s_mov_b32 s11, 0x41e6d4ca
	v_cmp_gt_f32_e32 vcc, s14, v103
	v_mul_f32_e32 v104, 0x4f800000, v103
	s_nop 0
	v_cndmask_b32_e32 v104, v103, v104, vcc
	v_sqrt_f32_e32 v103, v104
	s_nop 0
	v_add_u32_e32 v105, -1, v103
	v_fma_f32 v108, -v105, v103, v104
	v_cmp_ge_f32_e64 s[2:3], 0, v108
	v_add_u32_e32 v108, 1, v103
	s_nop 0
	v_cndmask_b32_e64 v105, v103, v105, s[2:3]
	v_fma_f32 v103, -v108, v103, v104
	v_cmp_lt_f32_e64 s[2:3], 0, v103
	s_nop 1
	v_cndmask_b32_e64 v103, v105, v108, s[2:3]
	v_mul_f32_e32 v105, 0x37800000, v103
	v_cndmask_b32_e32 v105, v103, v105, vcc
	v_mov_b32_e32 v103, 0x260
	v_cmp_class_f32_e32 vcc, v104, v103
	s_nop 1
	v_cndmask_b32_e32 v104, v105, v104, vcc
	v_add_f32_e32 v104, 0x322bcc77, v104
	v_div_scale_f32 v108, s[2:3], v104, v104, s11
	v_rcp_f32_e32 v105, v108
	s_nop 0
	v_fma_f32 v109, -v108, v105, 1.0
	v_fmac_f32_e32 v105, v109, v105
	v_div_scale_f32 v107, vcc, s11, v104, s11
	v_mul_f32_e32 v106, v107, v105
	v_fma_f32 v111, -v108, v106, v107
	v_fmac_f32_e32 v106, v111, v105
	v_fma_f32 v107, -v108, v106, v107
	s_nop 0
	v_div_fmas_f32 v109, v107, v105, v106
	v_div_fixup_f32 v109, v109, v104, s11
	v_lshlrev_b32_e32 v110, 2, v101
	ds_bpermute_b32 v108, v110, v109
	ds_bpermute_b32 v111, v110, v109 offset:64
	ds_bpermute_b32 v112, v110, v109 offset:128
	ds_bpermute_b32 v113, v110, v109 offset:192
	s_mul_i32 s2, s23, 0x1f80
	s_add_i32 s6, s8, s2
	s_movk_i32 s2, 0x88
	v_and_b32_e32 v66, 0x70, v100
	v_add_u32_e32 v71, s10, v66
	v_lshrrev_b32_e32 v67, 4, v100
	v_lshlrev_b32_e32 v67, 3, v67
	v_add_u32_e32 v72, s6, v67
	s_mov_b32 s34, 0x3d0df4e0
	v_mad_u32_u24 v120, v101, s2, v72
	ds_read_b128 v[114:117], v71 offset:8832
	s_waitcnt lgkmcnt(0)
	v_mul_f32_e32 v64, v114, v108
	v_mul_f32_e32 v65, v115, v108
	v_mul_f32_e32 v66, v116, v108
	v_mul_f32_e32 v67, v117, v108
	v_fmaak_f32 v60, v60, v64, 0xc1e6d4ca
	v_fmaak_f32 v61, v61, v65, 0xc1e6d4ca
	v_fmaak_f32 v62, v62, v66, 0xc1e6d4ca
	v_fmaak_f32 v63, v63, v67, 0xc1e6d4ca
	v_exp_f32_e32 v64, v60
	v_exp_f32_e32 v65, v61
	v_exp_f32_e32 v66, v62
	v_exp_f32_e32 v67, v63
	v_fma_f32 v60, v60, s34, 1.0
	v_fma_f32 v61, v61, s34, 1.0
	v_fma_f32 v62, v62, s34, 1.0
	v_fma_f32 v63, v63, s34, 1.0
	v_mul_f32_e32 v60, v64, v60
	v_mul_f32_e32 v61, v65, v61
	v_mul_f32_e32 v62, v66, v62
	v_mul_f32_e32 v63, v67, v63
	v_cvt_pk_bf16_f32 v68, v64, v65
	v_cvt_pk_bf16_f32 v69, v66, v67
	ds_write_b64 v120, v[68:69] offset:10240
	v_cvt_pk_bf16_f32 v72, v60, v61
	v_cvt_pk_bf16_f32 v73, v62, v63
	v_mul_f32_e32 v64, v114, v111
	v_mul_f32_e32 v65, v115, v111
	v_mul_f32_e32 v66, v116, v111
	v_mul_f32_e32 v67, v117, v111
	v_fmaak_f32 v56, v56, v64, 0xc1e6d4ca
	v_fmaak_f32 v57, v57, v65, 0xc1e6d4ca
	v_fmaak_f32 v58, v58, v66, 0xc1e6d4ca
	v_fmaak_f32 v59, v59, v67, 0xc1e6d4ca
	v_exp_f32_e32 v64, v56
	v_exp_f32_e32 v65, v57
	v_exp_f32_e32 v66, v58
	v_exp_f32_e32 v67, v59
	v_fma_f32 v56, v56, s34, 1.0
	v_fma_f32 v57, v57, s34, 1.0
	v_fma_f32 v58, v58, s34, 1.0
	v_fma_f32 v59, v59, s34, 1.0
	v_mul_f32_e32 v56, v64, v56
	v_mul_f32_e32 v57, v65, v57
	v_mul_f32_e32 v58, v66, v58
	v_mul_f32_e32 v59, v67, v59
	v_cvt_pk_bf16_f32 v68, v64, v65
	v_cvt_pk_bf16_f32 v69, v66, v67
	ds_write_b64 v120, v[68:69] offset:12416
	v_cvt_pk_bf16_f32 v74, v56, v57
	v_cvt_pk_bf16_f32 v75, v58, v59
	v_mul_f32_e32 v64, v114, v112
	v_mul_f32_e32 v65, v115, v112
	v_mul_f32_e32 v66, v116, v112
	v_mul_f32_e32 v67, v117, v112
	v_fmaak_f32 v52, v52, v64, 0xc1e6d4ca
	v_fmaak_f32 v53, v53, v65, 0xc1e6d4ca
	v_fmaak_f32 v54, v54, v66, 0xc1e6d4ca
	v_fmaak_f32 v55, v55, v67, 0xc1e6d4ca
	v_exp_f32_e32 v64, v52
	v_exp_f32_e32 v65, v53
	v_exp_f32_e32 v66, v54
	v_exp_f32_e32 v67, v55
	v_fma_f32 v52, v52, s34, 1.0
	v_fma_f32 v53, v53, s34, 1.0
	v_fma_f32 v54, v54, s34, 1.0
	v_fma_f32 v55, v55, s34, 1.0
	v_mul_f32_e32 v52, v64, v52
	v_mul_f32_e32 v53, v65, v53
	v_mul_f32_e32 v54, v66, v54
	v_mul_f32_e32 v55, v67, v55
	v_cvt_pk_bf16_f32 v68, v64, v65
	v_cvt_pk_bf16_f32 v69, v66, v67
	ds_write_b64 v120, v[68:69] offset:14592
	v_cvt_pk_bf16_f32 v76, v52, v53
	v_cvt_pk_bf16_f32 v77, v54, v55
	v_mul_f32_e32 v64, v114, v113
	v_mul_f32_e32 v65, v115, v113
	v_mul_f32_e32 v66, v116, v113
	v_mul_f32_e32 v67, v117, v113
	ds_read_b128 v[114:117], v71 offset:8896
	v_fmaak_f32 v48, v48, v64, 0xc1e6d4ca
	v_fmaak_f32 v49, v49, v65, 0xc1e6d4ca
	v_fmaak_f32 v50, v50, v66, 0xc1e6d4ca
	v_fmaak_f32 v51, v51, v67, 0xc1e6d4ca
	v_exp_f32_e32 v64, v48
	v_exp_f32_e32 v65, v49
	v_exp_f32_e32 v66, v50
	v_exp_f32_e32 v67, v51
	v_fma_f32 v48, v48, s34, 1.0
	v_fma_f32 v49, v49, s34, 1.0
	v_fma_f32 v50, v50, s34, 1.0
	v_fma_f32 v51, v51, s34, 1.0
	v_mul_f32_e32 v48, v64, v48
	v_mul_f32_e32 v49, v65, v49
	v_mul_f32_e32 v50, v66, v50
	v_mul_f32_e32 v51, v67, v51
	v_cvt_pk_bf16_f32 v68, v64, v65
	v_cvt_pk_bf16_f32 v69, v66, v67
	ds_write_b64 v120, v[68:69] offset:16768
	v_cvt_pk_bf16_f32 v78, v48, v49
	v_cvt_pk_bf16_f32 v79, v50, v51
	s_waitcnt lgkmcnt(0)
	v_mul_f32_e32 v64, v114, v108
	v_mul_f32_e32 v65, v115, v108
	v_mul_f32_e32 v66, v116, v108
	v_mul_f32_e32 v67, v117, v108
	v_fmaak_f32 v44, v44, v64, 0xc1e6d4ca
	v_fmaak_f32 v45, v45, v65, 0xc1e6d4ca
	v_fmaak_f32 v46, v46, v66, 0xc1e6d4ca
	v_fmaak_f32 v47, v47, v67, 0xc1e6d4ca
	v_exp_f32_e32 v64, v44
	v_exp_f32_e32 v65, v45
	v_exp_f32_e32 v66, v46
	v_exp_f32_e32 v67, v47
	v_fma_f32 v44, v44, s34, 1.0
	v_fma_f32 v45, v45, s34, 1.0
	v_fma_f32 v46, v46, s34, 1.0
	v_fma_f32 v47, v47, s34, 1.0
	v_mul_f32_e32 v44, v64, v44
	v_mul_f32_e32 v45, v65, v45
	v_mul_f32_e32 v46, v66, v46
	v_mul_f32_e32 v47, v67, v47
	v_cvt_pk_bf16_f32 v68, v64, v65
	v_cvt_pk_bf16_f32 v69, v66, v67
	ds_write_b64 v120, v[68:69] offset:10272
	v_cvt_pk_bf16_f32 v80, v44, v45
	v_cvt_pk_bf16_f32 v81, v46, v47
	v_mul_f32_e32 v64, v114, v111
	v_mul_f32_e32 v65, v115, v111
	v_mul_f32_e32 v66, v116, v111
	v_mul_f32_e32 v67, v117, v111
	v_fmaak_f32 v40, v40, v64, 0xc1e6d4ca
	v_fmaak_f32 v41, v41, v65, 0xc1e6d4ca
	v_fmaak_f32 v42, v42, v66, 0xc1e6d4ca
	v_fmaak_f32 v43, v43, v67, 0xc1e6d4ca
	v_exp_f32_e32 v64, v40
	v_exp_f32_e32 v65, v41
	v_exp_f32_e32 v66, v42
	v_exp_f32_e32 v67, v43
	v_fma_f32 v40, v40, s34, 1.0
	v_fma_f32 v41, v41, s34, 1.0
	v_fma_f32 v42, v42, s34, 1.0
	v_fma_f32 v43, v43, s34, 1.0
	v_mul_f32_e32 v40, v64, v40
	v_mul_f32_e32 v41, v65, v41
	v_mul_f32_e32 v42, v66, v42
	v_mul_f32_e32 v43, v67, v43
	v_cvt_pk_bf16_f32 v68, v64, v65
	v_cvt_pk_bf16_f32 v69, v66, v67
	ds_write_b64 v120, v[68:69] offset:12448
	v_cvt_pk_bf16_f32 v82, v40, v41
	v_cvt_pk_bf16_f32 v83, v42, v43
	v_mul_f32_e32 v64, v114, v112
	v_mul_f32_e32 v65, v115, v112
	v_mul_f32_e32 v66, v116, v112
	v_mul_f32_e32 v67, v117, v112
	v_fmaak_f32 v36, v36, v64, 0xc1e6d4ca
	v_fmaak_f32 v37, v37, v65, 0xc1e6d4ca
	v_fmaak_f32 v38, v38, v66, 0xc1e6d4ca
	v_fmaak_f32 v39, v39, v67, 0xc1e6d4ca
	v_exp_f32_e32 v64, v36
	v_exp_f32_e32 v65, v37
	v_exp_f32_e32 v66, v38
	v_exp_f32_e32 v67, v39
	v_fma_f32 v36, v36, s34, 1.0
	v_fma_f32 v37, v37, s34, 1.0
	v_fma_f32 v38, v38, s34, 1.0
	v_fma_f32 v39, v39, s34, 1.0
	v_mul_f32_e32 v36, v64, v36
	v_mul_f32_e32 v37, v65, v37
	v_mul_f32_e32 v38, v66, v38
	v_mul_f32_e32 v39, v67, v39
	v_cvt_pk_bf16_f32 v68, v64, v65
	v_cvt_pk_bf16_f32 v69, v66, v67
	ds_write_b64 v120, v[68:69] offset:14624
	v_cvt_pk_bf16_f32 v84, v36, v37
	v_cvt_pk_bf16_f32 v85, v38, v39
	v_mul_f32_e32 v64, v114, v113
	v_mul_f32_e32 v65, v115, v113
	v_mul_f32_e32 v66, v116, v113
	v_mul_f32_e32 v67, v117, v113
	ds_read_b128 v[114:117], v71 offset:8960
	v_fmaak_f32 v32, v32, v64, 0xc1e6d4ca
	v_fmaak_f32 v33, v33, v65, 0xc1e6d4ca
	v_fmaak_f32 v34, v34, v66, 0xc1e6d4ca
	v_fmaak_f32 v35, v35, v67, 0xc1e6d4ca
	v_exp_f32_e32 v64, v32
	v_exp_f32_e32 v65, v33
	v_exp_f32_e32 v66, v34
	v_exp_f32_e32 v67, v35
	v_fma_f32 v32, v32, s34, 1.0
	v_fma_f32 v33, v33, s34, 1.0
	v_fma_f32 v34, v34, s34, 1.0
	v_fma_f32 v35, v35, s34, 1.0
	v_mul_f32_e32 v32, v64, v32
	v_mul_f32_e32 v33, v65, v33
	v_mul_f32_e32 v34, v66, v34
	v_mul_f32_e32 v35, v67, v35
	v_cvt_pk_bf16_f32 v68, v64, v65
	v_cvt_pk_bf16_f32 v69, v66, v67
	ds_write_b64 v120, v[68:69] offset:16800
	v_cvt_pk_bf16_f32 v86, v32, v33
	v_cvt_pk_bf16_f32 v87, v34, v35
	s_waitcnt lgkmcnt(0)
	v_mul_f32_e32 v64, v114, v108
	v_mul_f32_e32 v65, v115, v108
	v_mul_f32_e32 v66, v116, v108
	v_mul_f32_e32 v67, v117, v108
	v_fmaak_f32 v28, v28, v64, 0xc1e6d4ca
	v_fmaak_f32 v29, v29, v65, 0xc1e6d4ca
	v_fmaak_f32 v30, v30, v66, 0xc1e6d4ca
	v_fmaak_f32 v31, v31, v67, 0xc1e6d4ca
	v_exp_f32_e32 v64, v28
	v_exp_f32_e32 v65, v29
	v_exp_f32_e32 v66, v30
	v_exp_f32_e32 v67, v31
	v_fma_f32 v28, v28, s34, 1.0
	v_fma_f32 v29, v29, s34, 1.0
	v_fma_f32 v30, v30, s34, 1.0
	v_fma_f32 v31, v31, s34, 1.0
	v_mul_f32_e32 v28, v64, v28
	v_mul_f32_e32 v29, v65, v29
	v_mul_f32_e32 v30, v66, v30
	v_mul_f32_e32 v31, v67, v31
	v_cvt_pk_bf16_f32 v68, v64, v65
	v_cvt_pk_bf16_f32 v69, v66, v67
	ds_write_b64 v120, v[68:69] offset:10304
	v_cvt_pk_bf16_f32 v88, v28, v29
	v_cvt_pk_bf16_f32 v89, v30, v31
	v_mul_f32_e32 v64, v114, v111
	v_mul_f32_e32 v65, v115, v111
	v_mul_f32_e32 v66, v116, v111
	v_mul_f32_e32 v67, v117, v111
	v_fmaak_f32 v24, v24, v64, 0xc1e6d4ca
	v_fmaak_f32 v25, v25, v65, 0xc1e6d4ca
	v_fmaak_f32 v26, v26, v66, 0xc1e6d4ca
	v_fmaak_f32 v27, v27, v67, 0xc1e6d4ca
	v_exp_f32_e32 v64, v24
	v_exp_f32_e32 v65, v25
	v_exp_f32_e32 v66, v26
	v_exp_f32_e32 v67, v27
	v_fma_f32 v24, v24, s34, 1.0
	v_fma_f32 v25, v25, s34, 1.0
	v_fma_f32 v26, v26, s34, 1.0
	v_fma_f32 v27, v27, s34, 1.0
	v_mul_f32_e32 v24, v64, v24
	v_mul_f32_e32 v25, v65, v25
	v_mul_f32_e32 v26, v66, v26
	v_mul_f32_e32 v27, v67, v27
	v_cvt_pk_bf16_f32 v68, v64, v65
	v_cvt_pk_bf16_f32 v69, v66, v67
	ds_write_b64 v120, v[68:69] offset:12480
	v_cvt_pk_bf16_f32 v90, v24, v25
	v_cvt_pk_bf16_f32 v91, v26, v27
	v_mul_f32_e32 v64, v114, v112
	v_mul_f32_e32 v65, v115, v112
	v_mul_f32_e32 v66, v116, v112
	v_mul_f32_e32 v67, v117, v112
	v_fmaak_f32 v20, v20, v64, 0xc1e6d4ca
	v_fmaak_f32 v21, v21, v65, 0xc1e6d4ca
	v_fmaak_f32 v22, v22, v66, 0xc1e6d4ca
	v_fmaak_f32 v23, v23, v67, 0xc1e6d4ca
	v_exp_f32_e32 v64, v20
	v_exp_f32_e32 v65, v21
	v_exp_f32_e32 v66, v22
	v_exp_f32_e32 v67, v23
	v_fma_f32 v20, v20, s34, 1.0
	v_fma_f32 v21, v21, s34, 1.0
	v_fma_f32 v22, v22, s34, 1.0
	v_fma_f32 v23, v23, s34, 1.0
	v_mul_f32_e32 v20, v64, v20
	v_mul_f32_e32 v21, v65, v21
	v_mul_f32_e32 v22, v66, v22
	v_mul_f32_e32 v23, v67, v23
	v_cvt_pk_bf16_f32 v68, v64, v65
	v_cvt_pk_bf16_f32 v69, v66, v67
	ds_write_b64 v120, v[68:69] offset:14656
	v_cvt_pk_bf16_f32 v92, v20, v21
	v_cvt_pk_bf16_f32 v93, v22, v23
	v_mul_f32_e32 v64, v114, v113
	v_mul_f32_e32 v65, v115, v113
	v_mul_f32_e32 v66, v116, v113
	v_mul_f32_e32 v67, v117, v113
	ds_read_b128 v[114:117], v71 offset:9024
	v_fmaak_f32 v16, v16, v64, 0xc1e6d4ca
	v_fmaak_f32 v17, v17, v65, 0xc1e6d4ca
	v_fmaak_f32 v18, v18, v66, 0xc1e6d4ca
	v_fmaak_f32 v19, v19, v67, 0xc1e6d4ca
	v_exp_f32_e32 v64, v16
	v_exp_f32_e32 v65, v17
	v_exp_f32_e32 v66, v18
	v_exp_f32_e32 v67, v19
	v_fma_f32 v16, v16, s34, 1.0
	v_fma_f32 v17, v17, s34, 1.0
	v_fma_f32 v18, v18, s34, 1.0
	v_fma_f32 v19, v19, s34, 1.0
	v_mul_f32_e32 v16, v64, v16
	v_mul_f32_e32 v17, v65, v17
	v_mul_f32_e32 v18, v66, v18
	v_mul_f32_e32 v19, v67, v19
	v_cvt_pk_bf16_f32 v68, v64, v65
	v_cvt_pk_bf16_f32 v69, v66, v67
	ds_write_b64 v120, v[68:69] offset:16832
	v_cvt_pk_bf16_f32 v94, v16, v17
	v_cvt_pk_bf16_f32 v95, v18, v19
	s_waitcnt lgkmcnt(0)
	v_mul_f32_e32 v64, v114, v108
	v_mul_f32_e32 v65, v115, v108
	v_mul_f32_e32 v66, v116, v108
	v_mul_f32_e32 v67, v117, v108
	v_fmaak_f32 v12, v12, v64, 0xc1e6d4ca
	v_fmaak_f32 v13, v13, v65, 0xc1e6d4ca
	v_fmaak_f32 v14, v14, v66, 0xc1e6d4ca
	v_fmaak_f32 v15, v15, v67, 0xc1e6d4ca
	v_exp_f32_e32 v64, v12
	v_exp_f32_e32 v65, v13
	v_exp_f32_e32 v66, v14
	v_exp_f32_e32 v67, v15
	v_fma_f32 v12, v12, s34, 1.0
	v_fma_f32 v13, v13, s34, 1.0
	v_fma_f32 v14, v14, s34, 1.0
	v_fma_f32 v15, v15, s34, 1.0
	v_mul_f32_e32 v12, v64, v12
	v_mul_f32_e32 v13, v65, v13
	v_mul_f32_e32 v14, v66, v14
	v_mul_f32_e32 v15, v67, v15
	v_cvt_pk_bf16_f32 v68, v64, v65
	v_cvt_pk_bf16_f32 v69, v66, v67
	ds_write_b64 v120, v[68:69] offset:10336
	v_cvt_pk_bf16_f32 v96, v12, v13
	v_cvt_pk_bf16_f32 v97, v14, v15
	v_mul_f32_e32 v64, v114, v111
	v_mul_f32_e32 v65, v115, v111
	v_mul_f32_e32 v66, v116, v111
	v_mul_f32_e32 v67, v117, v111
	v_fmaak_f32 v8, v8, v64, 0xc1e6d4ca
	v_fmaak_f32 v9, v9, v65, 0xc1e6d4ca
	v_fmaak_f32 v10, v10, v66, 0xc1e6d4ca
	v_fmaak_f32 v11, v11, v67, 0xc1e6d4ca
	v_exp_f32_e32 v64, v8
	v_exp_f32_e32 v65, v9
	v_exp_f32_e32 v66, v10
	v_exp_f32_e32 v67, v11
	v_fma_f32 v8, v8, s34, 1.0
	v_fma_f32 v9, v9, s34, 1.0
	v_fma_f32 v10, v10, s34, 1.0
	v_fma_f32 v11, v11, s34, 1.0
	v_mul_f32_e32 v8, v64, v8
	v_mul_f32_e32 v9, v65, v9
	v_mul_f32_e32 v10, v66, v10
	v_mul_f32_e32 v11, v67, v11
	v_cvt_pk_bf16_f32 v68, v64, v65
	v_cvt_pk_bf16_f32 v69, v66, v67
	ds_write_b64 v120, v[68:69] offset:12512
	v_cvt_pk_bf16_f32 v98, v8, v9
	v_cvt_pk_bf16_f32 v99, v10, v11
	v_mul_f32_e32 v64, v114, v112
	v_mul_f32_e32 v65, v115, v112
	v_mul_f32_e32 v66, v116, v112
	v_mul_f32_e32 v67, v117, v112
	v_fmaak_f32 v4, v4, v64, 0xc1e6d4ca
	v_fmaak_f32 v5, v5, v65, 0xc1e6d4ca
	v_fmaak_f32 v6, v6, v66, 0xc1e6d4ca
	v_fmaak_f32 v7, v7, v67, 0xc1e6d4ca
	v_exp_f32_e32 v64, v4
	v_exp_f32_e32 v65, v5
	v_exp_f32_e32 v66, v6
	v_exp_f32_e32 v67, v7
	v_fma_f32 v4, v4, s34, 1.0
	v_fma_f32 v5, v5, s34, 1.0
	v_fma_f32 v6, v6, s34, 1.0
	v_fma_f32 v7, v7, s34, 1.0
	v_mul_f32_e32 v4, v64, v4
	v_mul_f32_e32 v5, v65, v5
	v_mul_f32_e32 v6, v66, v6
	v_mul_f32_e32 v7, v67, v7
	v_cvt_pk_bf16_f32 v68, v64, v65
	v_cvt_pk_bf16_f32 v69, v66, v67
	ds_write_b64 v120, v[68:69] offset:14688
	v_cvt_pk_bf16_f32 v104, v4, v5
	v_cvt_pk_bf16_f32 v105, v6, v7
	v_mul_f32_e32 v64, v114, v113
	v_mul_f32_e32 v65, v115, v113
	v_mul_f32_e32 v66, v116, v113
	v_mul_f32_e32 v67, v117, v113
	v_fmaak_f32 v0, v0, v64, 0xc1e6d4ca
	v_fmaak_f32 v1, v1, v65, 0xc1e6d4ca
	v_fmaak_f32 v2, v2, v66, 0xc1e6d4ca
	v_fmaak_f32 v3, v3, v67, 0xc1e6d4ca
	v_exp_f32_e32 v64, v0
	v_exp_f32_e32 v65, v1
	v_exp_f32_e32 v66, v2
	v_exp_f32_e32 v67, v3
	v_fma_f32 v0, v0, s34, 1.0
	v_fma_f32 v1, v1, s34, 1.0
	v_fma_f32 v2, v2, s34, 1.0
	v_fma_f32 v3, v3, s34, 1.0
	v_mul_f32_e32 v0, v64, v0
	v_mul_f32_e32 v1, v65, v1
	v_mul_f32_e32 v2, v66, v2
	v_mul_f32_e32 v3, v67, v3
	v_cvt_pk_bf16_f32 v68, v64, v65
	v_cvt_pk_bf16_f32 v69, v66, v67
	ds_write_b64 v120, v[68:69] offset:16864
	v_cvt_pk_bf16_f32 v106, v0, v1
	v_cvt_pk_bf16_f32 v107, v2, v3
	s_movk_i32 s34, 0x88
	v_and_b32_e32 v64, 32, v100
	v_and_b32_e32 v66, 16, v100
	v_mad_u32_u24 v65, v101, s34, v64
	v_add_u32_e32 v65, s6, v65
	v_add_u32_e32 v67, v65, v66
	v_sub_u32_e32 v65, v65, v66
	v_lshrrev_b32_e32 v68, 1, v100
	v_and_b32_e32 v68, 16, v68
	v_bfe_u32 v69, v100, 2, 2
	v_or_b32_e32 v68, v68, v69
	v_and_b32_e32 v69, 3, v100
	v_lshlrev_b32_e32 v69, 3, v69
	v_mad_u32_u24 v68, v68, s34, v69
	v_add_u32_e32 v68, s6, v68
	s_movk_i32 s35, 0x44
	v_mul_u32_u24_e32 v66, s35, v66
	v_add_u32_e32 v69, v68, v66
	v_sub_u32_e32 v68, v68, v66
	ds_read_b64 v[0:1], v67 offset:10240
	ds_read_b64 v[2:3], v65 offset:10264
	ds_read_b64 v[4:5], v67 offset:10304
	ds_read_b64 v[6:7], v65 offset:10328
	ds_read_b64 v[8:9], v67 offset:12424
	ds_read_b64 v[10:11], v67 offset:12416
	ds_read_b64 v[12:13], v67 offset:12488
	ds_read_b64 v[14:15], v67 offset:12480
	ds_read_b64 v[16:17], v65 offset:14608
	ds_read_b64 v[18:19], v67 offset:14600
	ds_read_b64 v[20:21], v65 offset:14672
	ds_read_b64 v[22:23], v67 offset:14664
	ds_read_b64 v[24:25], v65 offset:16792
	ds_read_b64 v[26:27], v65 offset:16784
	ds_read_b64 v[28:29], v65 offset:16856
	ds_read_b64 v[30:31], v65 offset:16848
	ds_read_b64_tr_b16 v[32:33], v69 offset:10240
	ds_read_b64_tr_b16 v[34:35], v68 offset:11872
	ds_read_b64_tr_b16 v[36:37], v69 offset:14592
	ds_read_b64_tr_b16 v[38:39], v68 offset:16224
	ds_read_b64_tr_b16 v[40:41], v69 offset:10816
	ds_read_b64_tr_b16 v[42:43], v69 offset:10272
	ds_read_b64_tr_b16 v[44:45], v69 offset:15168
	ds_read_b64_tr_b16 v[46:47], v69 offset:14624
	ds_read_b64_tr_b16 v[48:49], v68 offset:11392
	ds_read_b64_tr_b16 v[50:51], v69 offset:10848
	ds_read_b64_tr_b16 v[52:53], v68 offset:15744
	ds_read_b64_tr_b16 v[54:55], v69 offset:15200
	ds_read_b64_tr_b16 v[56:57], v68 offset:11968
	ds_read_b64_tr_b16 v[58:59], v68 offset:11424
	ds_read_b64_tr_b16 v[60:61], v68 offset:16320
	ds_read_b64_tr_b16 v[62:63], v68 offset:15776
	ds_read2st64_b32 v[116:117], v102 offset0:22 offset1:23
	s_waitcnt lgkmcnt(0)
	ds_write_b64 v120, v[72:73] offset:10240
	ds_write_b64 v120, v[74:75] offset:12416
	ds_write_b64 v120, v[76:77] offset:14592
	ds_write_b64 v120, v[78:79] offset:16768
	ds_write_b64 v120, v[80:81] offset:10272
	ds_write_b64 v120, v[82:83] offset:12448
	ds_write_b64 v120, v[84:85] offset:14624
	ds_write_b64 v120, v[86:87] offset:16800
	ds_write_b64 v120, v[88:89] offset:10304
	ds_write_b64 v120, v[90:91] offset:12480
	ds_write_b64 v120, v[92:93] offset:14656
	ds_write_b64 v120, v[94:95] offset:16832
	ds_write_b64 v120, v[96:97] offset:10336
	ds_write_b64 v120, v[98:99] offset:12512
	ds_write_b64 v120, v[104:105] offset:14688
	ds_write_b64 v120, v[106:107] offset:16864
	v_and_b32_e32 v110, 1, v100
	v_cmp_eq_u32_e32 vcc, 0, v110
	v_mov_b32_e32 v110, 0xeeeeeeee
	v_mov_b32_e32 v111, 0x44444444
	s_mov_b32 s32, 0x2b8cbccc
	s_mov_b32 s33, 0
	v_cndmask_b32_e32 v64, v110, v111, vcc
	v_mov_b32_e32 v68, 0x3f803f80
	v_mov_b32_e32 v69, v68
	v_mov_b32_e32 v70, v68
	v_mov_b32_e32 v71, v68
	v_mov_b64_e32 v[72:73], s[32:33]
	v_mov_b64_e32 v[76:77], s[32:33]
	v_mov_b64_e32 v[80:81], s[32:33]
	v_mov_b64_e32 v[84:85], s[32:33]
	v_mov_b64_e32 v[88:89], s[32:33]
	v_mov_b64_e32 v[92:93], s[32:33]
	v_mov_b64_e32 v[96:97], s[32:33]
	v_mov_b64_e32 v[104:105], s[32:33]
	s_movk_i32 s30, 100
	v_mov_b32_e32 v122, 0
	v_mov_b32_e32 v121, 0
	s_waitcnt lgkmcnt(0)
	v_mov_b32_dpp v112, v116 quad_perm:[0,2,0,2] row_mask:0xf bank_mask:0xf
	v_mov_b32_dpp v113, v116 quad_perm:[1,3,1,3] row_mask:0xf bank_mask:0xf
	v_mov_b32_dpp v114, v117 quad_perm:[0,2,0,2] row_mask:0xf bank_mask:0xf
	v_mov_b32_dpp v115, v117 quad_perm:[1,3,1,3] row_mask:0xf bank_mask:0xf
	v_smfmac_f32_16x16x64_bf16 v[72:75], v[68:71], v[0:7], v64
	v_smfmac_f32_16x16x64_bf16 v[76:79], v[68:71], v[8:15], v64
	v_smfmac_f32_16x16x64_bf16 v[80:83], v[68:71], v[16:23], v64
	v_smfmac_f32_16x16x64_bf16 v[84:87], v[68:71], v[24:31], v64
	s_nop 0
.Lsk_loop:
	s_nop 3
	v_add_f32_dpp v108, v72, v73 quad_perm:[0,1,2,3] row_mask:0x1 bank_mask:0xf
	v_add_f32_dpp v108, v76, v77 quad_perm:[0,1,2,3] row_mask:0x2 bank_mask:0xf
	v_add_f32_dpp v108, v80, v81 quad_perm:[0,1,2,3] row_mask:0x4 bank_mask:0xf
	v_add_f32_dpp v108, v84, v85 quad_perm:[0,1,2,3] row_mask:0x8 bank_mask:0xf
	v_rcp_f32_e32 v109, v108
	v_mov_b64_e32 v[88:89], s[32:33]
	v_mov_b64_e32 v[92:93], s[32:33]
	v_mul_f32_dpp v110, v109, v114 quad_perm:[0,2,0,2] row_mask:0xf bank_mask:0xf
	v_mul_f32_dpp v111, v109, v115 quad_perm:[1,3,1,3] row_mask:0xf bank_mask:0xf
	v_cvt_pk_bf16_f32 v68, v110, v111
	v_mov_b64_e32 v[96:97], s[32:33]
	v_mov_b64_e32 v[104:105], s[32:33]
	v_mov_b32_dpp v69, v68 row_ror:4 row_mask:0xf bank_mask:0xf
	v_mov_b32_dpp v70, v68 row_ror:8 row_mask:0xf bank_mask:0xf
	v_mov_b32_dpp v71, v68 row_ror:12 row_mask:0xf bank_mask:0xf
	s_nop 1
	v_smfmac_f32_16x16x64_bf16 v[88:91], v[68:71], v[32:39], v64
	v_smfmac_f32_16x16x64_bf16 v[92:95], v[68:71], v[40:47], v64
	v_smfmac_f32_16x16x64_bf16 v[96:99], v[68:71], v[48:55], v64
	v_smfmac_f32_16x16x64_bf16 v[104:107], v[68:71], v[56:63], v64
	s_nop 4
	v_add_f32_dpp v108, v88, v89 quad_perm:[0,1,2,3] row_mask:0x1 bank_mask:0xf
	v_add_f32_dpp v108, v92, v93 quad_perm:[0,1,2,3] row_mask:0x2 bank_mask:0xf
	v_add_f32_dpp v108, v96, v97 quad_perm:[0,1,2,3] row_mask:0x4 bank_mask:0xf
	v_add_f32_dpp v108, v104, v105 quad_perm:[0,1,2,3] row_mask:0x8 bank_mask:0xf
	v_rcp_f32_e32 v109, v108
	v_mov_b64_e32 v[72:73], s[32:33]
	v_mov_b64_e32 v[76:77], s[32:33]
	v_mul_f32_dpp v110, v109, v112 quad_perm:[0,2,0,2] row_mask:0xf bank_mask:0xf
	v_mul_f32_dpp v111, v109, v113 quad_perm:[1,3,1,3] row_mask:0xf bank_mask:0xf
	v_cvt_pk_bf16_f32 v68, v110, v111
	v_mov_b64_e32 v[80:81], s[32:33]
	v_mov_b64_e32 v[84:85], s[32:33]
	v_mov_b32_dpp v69, v68 row_ror:4 row_mask:0xf bank_mask:0xf
	v_mov_b32_dpp v70, v68 row_ror:8 row_mask:0xf bank_mask:0xf
	v_mov_b32_dpp v71, v68 row_ror:12 row_mask:0xf bank_mask:0xf
	v_cmp_ne_u32_e32 vcc, v68, v122
	v_cmp_ne_u32_e64 s[36:37], v68, v121
	v_mov_b32_e32 v121, v122
	v_mov_b32_e32 v122, v68
	s_cmp_eq_u64 vcc, 0
	s_cselect_b32 s30, 1, s30
	s_add_i32 s38, s30, -1
	s_and_b32 s38, s38, 1
	s_add_i32 s38, s38, 1
	s_cmp_eq_u64 s[36:37], 0
	s_cselect_b32 s30, s38, s30
	s_add_i32 s30, s30, -1
	s_cmp_lg_u32 s30, 0
	v_smfmac_f32_16x16x64_bf16 v[72:75], v[68:71], v[0:7], v64
	v_smfmac_f32_16x16x64_bf16 v[76:79], v[68:71], v[8:15], v64
	v_smfmac_f32_16x16x64_bf16 v[80:83], v[68:71], v[16:23], v64
	v_smfmac_f32_16x16x64_bf16 v[84:87], v[68:71], v[24:31], v64
	s_cbranch_scc1 .Lsk_loop
	s_nop 3
	v_add_f32_dpp v108, v72, v73 quad_perm:[0,1,2,3] row_mask:0x1 bank_mask:0xf
	v_add_f32_dpp v108, v76, v77 quad_perm:[0,1,2,3] row_mask:0x2 bank_mask:0xf
	v_add_f32_dpp v108, v80, v81 quad_perm:[0,1,2,3] row_mask:0x4 bank_mask:0xf
	v_add_f32_dpp v108, v84, v85 quad_perm:[0,1,2,3] row_mask:0x8 bank_mask:0xf
	v_rcp_f32_e32 v109, v108
	s_mov_b32 s34, 0x3d0df4e0
	s_mov_b32 s35, s34
	v_mul_f32_e32 v118, v117, v109
	ds_read_b64 v[0:1], v67 offset:10240
	ds_read_b64 v[2:3], v65 offset:10264
	ds_read_b64 v[4:5], v67 offset:10304
	ds_read_b64 v[6:7], v65 offset:10328
	ds_read_b64 v[8:9], v67 offset:12424
	ds_read_b64 v[10:11], v67 offset:12416
	ds_read_b64 v[12:13], v67 offset:12488
	ds_read_b64 v[14:15], v67 offset:12480
	ds_read_b64 v[16:17], v65 offset:14608
	ds_read_b64 v[18:19], v67 offset:14600
	ds_read_b64 v[20:21], v65 offset:14672
	ds_read_b64 v[22:23], v67 offset:14664
	ds_read_b64 v[24:25], v65 offset:16792
	ds_read_b64 v[26:27], v65 offset:16784
	ds_read_b64 v[28:29], v65 offset:16856
	ds_read_b64 v[30:31], v65 offset:16848
	s_waitcnt lgkmcnt(0)
	v_mov_b64_e32 v[88:89], s[32:33]
	v_mov_b64_e32 v[92:93], s[32:33]
	v_mov_b64_e32 v[96:97], s[32:33]
	v_mov_b64_e32 v[104:105], s[32:33]
	s_nop 1
	v_smfmac_f32_16x16x64_bf16 v[88:91], v[68:71], v[0:7], v64
	v_smfmac_f32_16x16x64_bf16 v[92:95], v[68:71], v[8:15], v64
	v_smfmac_f32_16x16x64_bf16 v[96:99], v[68:71], v[16:23], v64
	v_smfmac_f32_16x16x64_bf16 v[104:107], v[68:71], v[24:31], v64
	s_nop 4
	v_add_f32_dpp v108, v88, v89 quad_perm:[0,1,2,3] row_mask:0x1 bank_mask:0xf
	v_add_f32_dpp v108, v92, v93 quad_perm:[0,1,2,3] row_mask:0x2 bank_mask:0xf
	v_add_f32_dpp v108, v96, v97 quad_perm:[0,1,2,3] row_mask:0x4 bank_mask:0xf
	v_add_f32_dpp v108, v104, v105 quad_perm:[0,1,2,3] row_mask:0x8 bank_mask:0xf
	v_add_f32_e32 v108, 0xab8cbccc, v108
	v_mul_f32_e32 v108, v118, v108
	s_nop 1
	v_add_f32_dpp v108, v108, v108 row_ror:8 row_mask:0xf bank_mask:0xf
	s_nop 1
	v_add_f32_dpp v108, v108, v108 row_ror:4 row_mask:0xf bank_mask:0xf
	s_nop 1
	v_add_f32_dpp v108, v108, v108 row_ror:2 row_mask:0xf bank_mask:0xf
	s_nop 1
	v_add_f32_dpp v108, v108, v108 row_ror:1 row_mask:0xf bank_mask:0xf
	s_nop 1
	v_mov_b32_e32 v109, v108
	s_nop 1
	v_permlane16_swap_b32_e32 v108, v109
	v_add_f32_e32 v108, v108, v109
	v_mov_b32_e32 v109, v108
	s_nop 1
	v_permlane32_swap_b32_e32 v108, v109
	v_add_f32_e32 v108, v108, v109
	v_cmp_eq_u32_e32 vcc, 0, v100
	s_and_saveexec_b64 s[0:1], vcc
	s_cbranch_execz .LBB1_38
	s_mul_i32 s0, s22, 5
	s_add_i32 s0, s0, s23
	s_mov_b32 s1, 0
	s_lshl_b64 s[0:1], s[0:1], 2
	s_add_u32 s0, s12, s0
	s_addc_u32 s1, s13, s1
	v_mov_b32_e32 v109, 0
	global_store_dword v109, v108, s[0:1]
